# speedup vs baseline: 1.0046x; 1.0046x over previous
.Lh_nocs:
	s_mov_b64 exec, s[6:7]
	v_subrev_u32_e32 v69, 0x200, v0
	v_cmp_gt_u32_e32 vcc, 10, v69
	s_and_saveexec_b64 s[4:5], vcc
	s_cbranch_execz .LBB2_30
	v_lshlrev_b32_e32 v21, 2, v69
	v_lshlrev_b32_e32 v18, 8, v69
	global_load_dword v20, v21, s[16:17]
	global_load_dwordx3 v[14:16], v18, s[22:23] offset:52 nt
	global_load_dwordx4 v[2:5], v18, s[22:23] offset:36 nt
	global_load_dwordx4 v[6:9], v18, s[22:23] offset:20 nt
	global_load_dwordx4 v[10:13], v18, s[22:23] offset:4 nt
	global_load_dword v19, v18, s[22:23] nt
	global_load_dword v8, v21, s[12:13]
	s_waitcnt vmcnt(0)
	v_add_u32_e32 v22, 0x7f, v20
	v_ashrrev_i32_e32 v22, 7, v22
	v_cmp_lt_i32_e32 vcc, 0, v22
	v_add_f32_e32 v19, 0, v19
	s_nop 0
	v_cndmask_b32_e32 v19, 0, v19, vcc
	v_cmp_lt_i32_e32 vcc, 1, v22
	s_nop 0
	v_cndmask_b32_e32 v10, 0, v10, vcc
	v_cmp_lt_i32_e32 vcc, 2, v22
	v_add_f32_e32 v10, v19, v10
	s_nop 0
	v_cndmask_b32_e32 v11, 0, v11, vcc
	v_cmp_lt_i32_e32 vcc, 3, v22
	v_add_f32_e32 v10, v10, v11
	s_nop 0
	v_cndmask_b32_e32 v11, 0, v12, vcc
	v_cmp_lt_i32_e32 vcc, 4, v22
	v_add_f32_e32 v10, v10, v11
	s_nop 0
	v_cndmask_b32_e32 v11, 0, v13, vcc
	v_cmp_lt_i32_e32 vcc, 5, v22
	v_add_f32_e32 v10, v10, v11
	s_nop 0
	v_cndmask_b32_e32 v6, 0, v6, vcc
	v_cmp_lt_i32_e32 vcc, 6, v22
	v_add_f32_e32 v6, v10, v6
	s_nop 0
	v_cndmask_b32_e32 v7, 0, v7, vcc
	v_cmp_lt_i32_e32 vcc, 7, v22
	v_add_f32_e32 v6, v6, v7
	s_nop 0
	v_cndmask_b32_e32 v7, 0, v8, vcc
	v_cmp_lt_i32_e32 vcc, 8, v22
	v_add_f32_e32 v6, v6, v7
	s_nop 0
	v_cndmask_b32_e32 v7, 0, v9, vcc
	v_cmp_lt_i32_e32 vcc, 9, v22
	v_add_f32_e32 v6, v6, v7
	s_nop 0
	v_cndmask_b32_e32 v2, 0, v2, vcc
	v_cmp_lt_i32_e32 vcc, 10, v22
	v_add_f32_e32 v2, v6, v2
	s_nop 0
	v_cndmask_b32_e32 v3, 0, v3, vcc
	v_cmp_lt_i32_e32 vcc, 11, v22
	v_add_f32_e32 v2, v2, v3
	s_nop 0
	v_cndmask_b32_e32 v3, 0, v4, vcc
	v_cmp_lt_i32_e32 vcc, 12, v22
	v_add_f32_e32 v2, v2, v3
	s_nop 0
	v_cndmask_b32_e32 v3, 0, v5, vcc
	v_cmp_lt_i32_e32 vcc, 13, v22
	v_add_f32_e32 v2, v2, v3
	s_nop 0
	v_cndmask_b32_e32 v3, 0, v14, vcc
	v_cmp_lt_i32_e32 vcc, 14, v22
	v_add_f32_e32 v2, v2, v3
	s_nop 0
	v_cndmask_b32_e32 v3, 0, v15, vcc
	v_cmp_lt_i32_e32 vcc, 15, v22
	v_add_f32_e32 v2, v2, v3
	s_nop 0
	v_cndmask_b32_e32 v3, 0, v16, vcc
	v_add_f32_e32 v4, v2, v3
	v_cmp_lt_i32_e32 vcc, 16, v22
	s_and_saveexec_b64 s[6:7], vcc
	s_cbranch_execz .LBB2_29
	v_mov_b32_e32 v19, 0
	v_lshl_add_u64 v[2:3], s[22:23], 0, v[18:19]
	v_lshl_add_u64 v[2:3], v[2:3], 0, 64
	v_add_u32_e32 v5, -16, v22
	s_mov_b64 s[22:23], 0

.Lmf_skip:
	s_cmp_lg_u32 s3, 8
	s_cbranch_scc1 .Lsp_skip
	s_waitcnt vmcnt(0)
	v_add_f32_dpp v54, v9, v9 quad_perm:[1,0,3,2] row_mask:0xf bank_mask:0xf bound_ctrl:1
	v_add_f32_dpp v55, v8, v8 quad_perm:[1,0,3,2] row_mask:0xf bank_mask:0xf bound_ctrl:1
	s_nop 0
	v_add_f32_dpp v54, v54, v54 quad_perm:[2,3,0,1] row_mask:0xf bank_mask:0xf bound_ctrl:1
	v_add_f32_dpp v55, v55, v55 quad_perm:[2,3,0,1] row_mask:0xf bank_mask:0xf bound_ctrl:1
	s_nop 0
	v_add_f32_dpp v54, v54, v54 row_half_mirror row_mask:0xf bank_mask:0xf bound_ctrl:1
	v_add_f32_dpp v55, v55, v55 row_half_mirror row_mask:0xf bank_mask:0xf bound_ctrl:1
	s_nop 0
	v_add_f32_dpp v54, v54, v54 row_mirror row_mask:0xf bank_mask:0xf bound_ctrl:1
	v_add_f32_dpp v55, v55, v55 row_mirror row_mask:0xf bank_mask:0xf bound_ctrl:1
	s_nop 0
	v_readlane_b32 s6, v54, 0
	v_readlane_b32 s8, v54, 16
	v_readlane_b32 s7, v54, 32
	v_readlane_b32 s9, v54, 48
	v_readlane_b32 s10, v55, 0
	v_readlane_b32 s12, v55, 16
	v_readlane_b32 s11, v55, 32
	v_readlane_b32 s13, v55, 48
	v_mov_b32_e32 v56, s8
	v_mov_b32_e32 v57, s9
	v_pk_add_f32 v[56:57], s[6:7], v[56:57]
	v_mov_b32_e32 v58, s12
	v_mov_b32_e32 v59, s13
	v_pk_add_f32 v[58:59], s[10:11], v[58:59]
	v_add_f32_e32 v56, v56, v57
	v_add_f32_e32 v57, v58, v59
	s_mov_b32 s3, 0x41200000
	v_div_scale_f32 v58, s[12:13], s3, s3, v57
	v_rcp_f32_e32 v59, v58
	s_nop 0
	v_fma_f32 v60, -v58, v59, 1.0
	v_fmac_f32_e32 v59, v60, v59
	v_div_scale_f32 v60, vcc, v57, s3, v57
	v_mul_f32_e32 v61, v60, v59
	v_fma_f32 v62, -v58, v61, v60
	v_fmac_f32_e32 v61, v62, v59
	v_fma_f32 v58, -v58, v61, v60
	v_div_scale_f32 v60, s[12:13], s3, s3, v56
	v_rcp_f32_e32 v62, v60
	v_div_fmas_f32 v58, v58, v59, v61
	v_div_fixup_f32 v57, v58, s3, v57
	s_mov_b32 s14, 0x322bcc77
	v_fma_f32 v58, -v60, v62, 1.0
	v_fmac_f32_e32 v62, v58, v62
	v_div_scale_f32 v58, vcc, v56, s3, v56
	v_mul_f32_e32 v59, v58, v62
	v_fma_f32 v61, -v60, v59, v58
	v_fmac_f32_e32 v59, v61, v62
	v_fma_f32 v58, -v60, v59, v58
	v_div_fmas_f32 v58, v58, v62, v59
	v_div_fixup_f32 v56, v58, s3, v56
	v_pk_add_f32 v[56:57], v[56:57], s[14:15] op_sel_hi:[1,0]
	s_nop 0
	v_div_scale_f32 v58, s[12:13], v57, v57, v8
	v_rcp_f32_e32 v59, v58
	s_nop 0
	v_fma_f32 v60, -v58, v59, 1.0
	v_fmac_f32_e32 v59, v60, v59
	v_div_scale_f32 v60, vcc, v8, v57, v8
	v_mul_f32_e32 v61, v60, v59
	v_fma_f32 v62, -v58, v61, v60
	v_fmac_f32_e32 v61, v62, v59
	v_fma_f32 v58, -v58, v61, v60
	v_div_scale_f32 v60, s[12:13], v56, v56, v9
	v_rcp_f32_e32 v62, v60
	v_div_fmas_f32 v58, v58, v59, v61
	v_div_fixup_f32 v57, v58, v57, v8
	v_fma_f32 v58, -v60, v62, 1.0
	v_fmac_f32_e32 v62, v58, v62
	v_div_scale_f32 v58, vcc, v9, v56, v9
	v_mul_f32_e32 v59, v58, v62
	v_fma_f32 v61, -v60, v59, v58
	v_fmac_f32_e32 v59, v61, v62
	v_fma_f32 v58, -v60, v59, v58
	v_div_fmas_f32 v58, v58, v62, v59
	v_div_fixup_f32 v56, v58, v56, v9
	v_sub_f32_e32 v56, v56, v57
	v_mul_f32_e32 v57, 0.5, v56
	v_mul_f32_e32 v56, v56, v57
	v_div_scale_f32 v57, s[12:13], s3, s3, v56
	v_rcp_f32_e32 v58, v57
	s_nop 0
	v_fma_f32 v59, -v57, v58, 1.0
	v_fmac_f32_e32 v58, v59, v58
	v_div_scale_f32 v59, vcc, v56, s3, v56
	v_mul_f32_e32 v60, v59, v58
	v_fma_f32 v61, -v57, v60, v59
	v_fmac_f32_e32 v60, v61, v58
	v_fma_f32 v57, -v57, v60, v59
	v_div_fmas_f32 v57, v57, v58, v60
	v_div_fixup_f32 v56, v57, s3, v56
	s_nop 1
	v_add_f32_dpp v56, v56, v56 quad_perm:[1,0,3,2] row_mask:0xf bank_mask:0xf bound_ctrl:1
	s_nop 1
	v_add_f32_dpp v56, v56, v56 quad_perm:[2,3,0,1] row_mask:0xf bank_mask:0xf bound_ctrl:1
	s_nop 1
	v_add_f32_dpp v56, v56, v56 row_half_mirror row_mask:0xf bank_mask:0xf bound_ctrl:1
	s_nop 1
	v_add_f32_dpp v56, v56, v56 row_mirror row_mask:0xf bank_mask:0xf bound_ctrl:1
	s_nop 0
	v_readlane_b32 s6, v56, 0
	v_readlane_b32 s8, v56, 16
	v_readlane_b32 s7, v56, 32
	v_readlane_b32 s9, v56, 48
	v_cmp_eq_u32_e32 vcc, 0, v1
	s_nop 1
	v_mov_b32_e32 v56, s8
	v_mov_b32_e32 v57, s9
	v_pk_add_f32 v[56:57], s[6:7], v[56:57]
	s_nop 0
	v_add_f32_e32 v56, v56, v57
	s_and_saveexec_b64 s[6:7], vcc
	v_mov_b32_e32 v57, 0
	global_atomic_add_f32 v57, v56, s[28:29]
	s_mov_b64 exec, s[6:7]
